# P7 router: 64-token units mapped to the XCD that produced their x2 rows in P6
# speedup vs baseline: 1.0047x; 1.0047x over previous
.LBB0_1164:
	s_or_b64 exec, exec, s[4:5]
	v_readlane_b32 s4, v251, 8
	s_add_u32 s18, s84, 0x45000000
	v_readlane_b32 s5, v251, 9
	v_mov_b32_e32 v2, v0
	s_addc_u32 s19, s85, 0
	s_and_b64 vcc, exec, s[4:5]
	s_waitcnt lgkmcnt(0)
	s_barrier
	s_cbranch_vccnz .LBB0_1266
	v_and_b32_e32 v6, 7, v2
	v_mbcnt_hi_u32_b32 v10, -1, v228
	v_lshlrev_b32_e32 v4, 4, v6
	v_mov_b32_e32 v5, 0
	v_and_b32_e32 v7, 64, v10
	v_lshl_add_u64 v[198:199], s[6:7], 0, v[4:5]
	v_xor_b32_e32 v4, 1, v10
	v_add_u32_e32 v11, 64, v7
	v_cmp_lt_i32_e32 vcc, v4, v11
	v_readlane_b32 s23, v252, 6
	s_add_i32 s8, 0, 0x10e00
	v_cndmask_b32_e32 v4, v10, v4, vcc
	v_lshlrev_b32_e32 v230, 2, v4
	v_xor_b32_e32 v4, 2, v10
	v_cmp_lt_i32_e32 vcc, v4, v11
	s_lshl_b32 s22, s23, 5
	v_and_b32_e32 v1, 15, v2
	v_cndmask_b32_e32 v4, v10, v4, vcc
	v_lshlrev_b32_e32 v231, 2, v4
	v_xor_b32_e32 v4, 4, v10
	v_bfe_u32 v3, v2, 3, 3
	v_cmp_lt_i32_e32 vcc, v4, v11
	s_add_i32 s6, s8, s22
	s_mov_b32 s21, 0
	v_cndmask_b32_e32 v4, v10, v4, vcc
	v_lshl_add_u32 v233, v3, 2, s6
	s_lshl_b32 s20, s23, 8
	s_lshl_b32 s6, s23, 9
	v_lshlrev_b32_e32 v8, 12, v1
	v_mov_b32_e32 v9, v5
	v_lshlrev_b32_e32 v232, 2, v4
	s_mov_b32 s7, s21
	s_add_u32 s0, s0, s6
	v_and_b32_e32 v4, 48, v2
	v_lshl_add_u64 v[8:9], s[84:85], 0, v[8:9]
	v_cmp_eq_u32_e64 s[4:5], 0, v6
	s_addc_u32 s1, s1, 0
	v_lshlrev_b32_e32 v6, 1, v4
	v_mov_b32_e32 v7, v5
	v_lshl_add_u64 v[8:9], v[8:9], 0, s[6:7]
	v_lshl_add_u64 v[200:201], s[0:1], 0, v[6:7]
	v_lshl_add_u64 v[6:7], v[8:9], 0, v[6:7]
	s_mov_b64 s[0:1], 0x210000
	v_lshl_add_u64 v[202:203], v[6:7], 0, s[0:1]
	s_mov_b64 s[0:1], 0x230000
	v_lshl_add_u64 v[204:205], v[6:7], 0, s[0:1]
	s_lshl_b64 s[0:1], s[20:21], 2
	s_add_u32 s0, s66, s0
	s_addc_u32 s1, s67, s1
	v_lshlrev_b32_e32 v8, 2, v4
	v_mov_b32_e32 v9, v5
	v_lshl_add_u64 v[206:207], s[0:1], 0, v[8:9]
	s_add_u32 s0, s84, s20
	s_addc_u32 s1, s85, 0
	v_lshl_or_b32 v229, s23, 3, v3
	v_lshl_add_u64 v[8:9], s[0:1], 0, v[4:5]
	s_mov_b64 s[0:1], 0x35400000
	v_lshlrev_b32_e32 v3, 2, v1
	v_lshl_add_u64 v[208:209], v[8:9], 0, s[0:1]
	v_add_u32_e32 v234, s8, v3
	s_mov_b64 s[0:1], 0x220000
	v_add_u32_e32 v8, 0, v3
	v_xor_b32_e32 v3, 16, v10
	v_lshl_add_u64 v[210:211], v[6:7], 0, s[0:1]
	s_mov_b64 s[0:1], 0x240000
	v_cmp_lt_i32_e32 vcc, v3, v11
	v_lshl_add_u64 v[212:213], v[6:7], 0, s[0:1]
	v_readlane_b32 s0, v252, 0
	v_cndmask_b32_e32 v3, v10, v3, vcc
	s_and_b32 s0, s0, 0x1ffffc0
	v_lshrrev_b32_e32 v4, 2, v2
	v_lshlrev_b32_e32 v236, 2, v3
	v_xor_b32_e32 v3, 8, v10
	v_and_or_b32 v4, v4, 12, s0
	v_cmp_lt_i32_e32 vcc, v3, v11
	s_movk_i32 s0, 0x100
	v_lshlrev_b32_e32 v6, 6, v2
	v_bfe_u32 v9, v2, 5, 1
	v_and_b32_e32 v235, 31, v2
	v_cndmask_b32_e32 v3, v10, v3, vcc
	v_cmp_gt_i32_e64 s[14:15], 32, v2
	v_cmp_gt_i32_e64 s[16:17], s0, v2
	v_lshlrev_b32_e32 v10, 2, v2
	s_add_i32 s0, 0, 0x10200
	v_ashrrev_i32_e32 v7, 31, v6
	v_ashrrev_i32_e32 v240, 2, v2
	v_lshlrev_b32_e32 v2, 4, v2
	v_lshlrev_b32_e32 v237, 2, v3
	v_add_u32_e32 v239, s0, v10
	v_lshl_add_u64 v[6:7], v[6:7], 2, s[84:85]
	s_mov_b64 s[0:1], 0x8000
	v_and_b32_e32 v2, 48, v2
	v_mov_b32_e32 v3, v5
	v_lshl_add_u64 v[216:217], v[6:7], 0, s[0:1]
	v_lshl_add_u64 v[2:3], s[84:85], 0, v[2:3]
	s_mov_b64 s[0:1], 0x45200000
	v_lshl_add_u64 v[218:219], v[2:3], 0, s[0:1]
	v_lshl_or_b32 v2, v9, 2, s22
	s_add_i32 s0, 0, 0x10600
	v_add_lshl_u32 v242, v2, v235, 2
	v_add_u32_e32 v243, 0x10e00, v2
	v_lshlrev_b32_e32 v2, 7, v9
	v_lshlrev_b32_e32 v12, 7, v4
	v_lshlrev_b32_e32 v4, 2, v235
	s_add_i32 s33, 0, 0x10a00
	v_add_u32_e32 v241, s0, v10
	v_lshl_or_b32 v2, s23, 10, v2
	s_movk_i32 s0, 0x200
	v_cmp_gt_u32_e64 s[6:7], 4, v235
	v_cmp_eq_u32_e64 s[8:9], 0, v235
	v_cmp_eq_u32_e64 s[10:11], 1, v235
	v_cmp_eq_u32_e64 s[12:13], 2, v235
	v_lshl_add_u64 v[214:215], s[70:71], 0, v[4:5]
	v_add_u32_e32 v238, s33, v10
	v_or3_b32 v244, v2, v4, s0
	v_mov_b32_e32 v245, 0x3727c5ac
	s_mov_b64 s[22:23], 0x10000
	s_mov_b32 s40, 0x10000
	s_mov_b64 s[24:25], 0x20000
	s_mov_b32 s41, 0x20000
	s_mov_b64 s[26:27], 0x30000
	s_mov_b32 s42, 0x30000
	s_mov_b64 s[28:29], 0x10080
	s_mov_b64 s[30:31], 0x20080
	s_mov_b64 s[34:35], 0x30080
	s_mov_b32 s43, 0x8000
	s_mov_b32 s44, 0x18000
	v_add_u32_e32 v246, v8, v12
	v_mov_b32_e32 v247, 1
	v_mov_b32_e32 v248, 0xff800000
	s_mov_b32 s45, s96
	v_readlane_b32 s100, v252, 41
	s_nop 3
	s_cmpk_lg_i32 s100, 0x100
	s_cbranch_scc1 .Lmy_p7_nomap
	s_and_b32 s45, s96, 7
	s_lshl_b32 s45, s45, 5
	s_lshr_b32 s100, s96, 3
	s_add_i32 s45, s45, s100
.Lmy_p7_nomap:
	s_branch .LBB0_1167
.LBB0_1166:
	s_or_b64 exec, exec, s[0:1]
	v_readlane_b32 s0, v252, 41
	s_add_i32 s45, s45, s0
	s_cmpk_lt_i32 s45, 0x100
	s_barrier
	s_cbranch_scc0 .LBB0_1265
